# GLU epilogue: touch-prefetch of the tile's y fragments before the serial load/store chain
# baseline (speedup 1.0000x reference)
.LBB0_2224:
	v_mbcnt_lo_u32_b32 v152, -1, 0
	v_mbcnt_hi_u32_b32 v152, -1, v152
	s_add_u32 s22, s22, s43
	v_and_or_b32 v136, v152, 15, s42
	v_lshlrev_b64 v[146:147], 10, v[136:137]
	v_lshrrev_b32_e32 v136, 1, v152
	v_and_b32_e32 v136, 24, v136
	s_addc_u32 s23, s23, 0
	v_lshl_add_u64 v[152:153], s[22:23], 0, v[136:137]
	v_lshl_add_u64 v[146:147], v[152:153], 0, v[146:147]
	v_lshlrev_b64 v[156:157], 1, v[146:147]
	v_lshl_add_u64 v[146:147], s[2:3], 0, v[156:157]
	global_load_dwordx4 v[152:155], v[146:147], off
	s_mov_b32 s98, 0x8000
	s_mov_b32 s99, 0
	s_mov_b32 s100, 0x28000
	s_mov_b32 s101, 0
	global_load_dword v160, v[146:147], off offset:256
	v_lshl_add_u64 v[214:215], v[146:147], 0, s[98:99]
	global_load_dword v161, v[214:215], off
	global_load_dword v162, v[214:215], off offset:256
	v_lshl_add_u64 v[214:215], v[214:215], 0, s[98:99]
	global_load_dword v163, v[214:215], off
	global_load_dword v164, v[214:215], off offset:256
	v_lshl_add_u64 v[214:215], v[214:215], 0, s[98:99]
	global_load_dword v165, v[214:215], off
	global_load_dword v166, v[214:215], off offset:256
	v_lshl_add_u64 v[214:215], v[214:215], 0, s[100:101]
	global_load_dword v167, v[214:215], off
	global_load_dword v168, v[214:215], off offset:256
	v_lshl_add_u64 v[214:215], v[214:215], 0, s[98:99]
	global_load_dword v169, v[214:215], off
	global_load_dword v170, v[214:215], off offset:256
	v_lshl_add_u64 v[214:215], v[214:215], 0, s[98:99]
	global_load_dword v171, v[214:215], off
	global_load_dword v172, v[214:215], off offset:256
	v_lshl_add_u64 v[214:215], v[214:215], 0, s[98:99]
	global_load_dword v173, v[214:215], off
	global_load_dword v174, v[214:215], off offset:256
	v_mul_f32_e32 v124, 0xbfb8aa3b, v124
	v_mul_f32_e32 v125, 0xbfb8aa3b, v125
	v_mul_f32_e32 v126, 0xbfb8aa3b, v126
	v_mul_f32_e32 v127, 0xbfb8aa3b, v127
	v_mul_f32_e32 v123, 0xbfb8aa3b, v123
	v_mul_f32_e32 v120, 0xbfb8aa3b, v120
	v_mul_f32_e32 v121, 0xbfb8aa3b, v121
	v_mul_f32_e32 v122, 0xbfb8aa3b, v122
	v_exp_f32_e32 v124, v124
	v_exp_f32_e32 v125, v125
	v_exp_f32_e32 v126, v126
	v_exp_f32_e32 v127, v127
	v_exp_f32_e32 v123, v123
	v_exp_f32_e32 v120, v120
	v_exp_f32_e32 v121, v121
	v_exp_f32_e32 v122, v122
	v_add_f32_e32 v124, 1.0, v124
	v_add_f32_e32 v125, 1.0, v125
	v_add_f32_e32 v126, 1.0, v126
	v_add_f32_e32 v127, 1.0, v127
	v_add_f32_e32 v123, 1.0, v123
	v_add_f32_e32 v120, 1.0, v120
	v_add_f32_e32 v121, 1.0, v121
	v_add_f32_e32 v122, 1.0, v122
	v_rcp_f32_e32 v124, v124
	v_rcp_f32_e32 v125, v125
	v_rcp_f32_e32 v126, v126
	v_rcp_f32_e32 v127, v127
	v_rcp_f32_e32 v123, v123
	v_rcp_f32_e32 v120, v120
	v_rcp_f32_e32 v121, v121
	v_rcp_f32_e32 v122, v122
	v_mul_f32_e32 v116, 0xbfb8aa3b, v116
	v_mul_f32_e32 v117, 0xbfb8aa3b, v117
	v_mul_f32_e32 v118, 0xbfb8aa3b, v118
	v_mul_f32_e32 v119, 0xbfb8aa3b, v119
	v_mul_f32_e32 v112, 0xbfb8aa3b, v112
	v_mul_f32_e32 v113, 0xbfb8aa3b, v113
	v_mul_f32_e32 v114, 0xbfb8aa3b, v114
	v_mul_f32_e32 v115, 0xbfb8aa3b, v115
	v_exp_f32_e32 v116, v116
	v_exp_f32_e32 v117, v117
	v_exp_f32_e32 v118, v118
	v_exp_f32_e32 v119, v119
	v_exp_f32_e32 v112, v112
	v_exp_f32_e32 v113, v113
	v_exp_f32_e32 v114, v114
	v_exp_f32_e32 v115, v115
	v_add_f32_e32 v116, 1.0, v116
	v_add_f32_e32 v117, 1.0, v117
	v_add_f32_e32 v118, 1.0, v118
	v_add_f32_e32 v119, 1.0, v119
	v_add_f32_e32 v114, 1.0, v114
	v_add_f32_e32 v115, 1.0, v115
	v_rcp_f32_e32 v116, v116
	v_rcp_f32_e32 v117, v117
	v_rcp_f32_e32 v118, v118
	v_rcp_f32_e32 v119, v119
	v_rcp_f32_e32 v114, v114
	v_rcp_f32_e32 v115, v115
	v_mul_f32_e32 v108, 0xbfb8aa3b, v108
	v_mul_f32_e32 v109, 0xbfb8aa3b, v109
	v_mul_f32_e32 v110, 0xbfb8aa3b, v110
	v_mul_f32_e32 v111, 0xbfb8aa3b, v111
	v_mul_f32_e32 v107, 0xbfb8aa3b, v107
	v_mul_f32_e32 v104, 0xbfb8aa3b, v104
	v_mul_f32_e32 v105, 0xbfb8aa3b, v105
	v_mul_f32_e32 v106, 0xbfb8aa3b, v106
	v_exp_f32_e32 v108, v108
	v_exp_f32_e32 v109, v109
	v_exp_f32_e32 v110, v110
	v_exp_f32_e32 v111, v111
	v_exp_f32_e32 v107, v107
	v_exp_f32_e32 v104, v104
	v_exp_f32_e32 v105, v105
	v_exp_f32_e32 v106, v106
	v_add_f32_e32 v108, 1.0, v108
	v_add_f32_e32 v109, 1.0, v109
	v_add_f32_e32 v110, 1.0, v110
	s_waitcnt vmcnt(0)
	v_lshlrev_b32_e32 v136, 16, v152
	v_and_b32_e32 v152, 0xffff0000, v152
	v_lshlrev_b32_e32 v158, 16, v153
	v_and_b32_e32 v153, 0xffff0000, v153
	v_lshlrev_b32_e32 v160, 16, v155
	v_and_b32_e32 v155, 0xffff0000, v155
	v_lshlrev_b32_e32 v159, 16, v154
	v_and_b32_e32 v154, 0xffff0000, v154
	v_mul_f32_e32 v124, v124, v136
	v_mul_f32_e32 v125, v125, v152
	v_mul_f32_e32 v126, v126, v158
	v_mul_f32_e32 v127, v127, v153
	v_mul_f32_e32 v123, v123, v155
	v_mul_f32_e32 v136, v120, v159
	v_mul_f32_e32 v152, v121, v154
	v_mul_f32_e32 v153, v122, v160
	v_cvt_pk_bf16_f32 v120, v124, v125
	v_cvt_pk_bf16_f32 v121, v126, v127
	v_cvt_pk_bf16_f32 v122, v136, v152
	v_cvt_pk_bf16_f32 v123, v153, v123
	global_load_dwordx4 v[124:127], v[146:147], off offset:256
	v_add_f32_e32 v136, 1.0, v112
	v_add_f32_e32 v152, 1.0, v113
	v_rcp_f32_e32 v136, v136
	v_rcp_f32_e32 v154, v152
	v_lshl_add_u64 v[112:113], s[6:7], 0, v[156:157]
	v_add_co_u32_e32 v152, vcc, s47, v146
	global_store_dwordx4 v[112:113], v[120:123], off
	s_nop 0
	v_addc_co_u32_e32 v153, vcc, 0, v147, vcc
	v_add_f32_e32 v111, 1.0, v111
	v_add_f32_e32 v107, 1.0, v107
	v_add_f32_e32 v104, 1.0, v104
	v_add_f32_e32 v105, 1.0, v105
	v_add_f32_e32 v106, 1.0, v106
	v_rcp_f32_e32 v108, v108
	v_rcp_f32_e32 v109, v109
	v_rcp_f32_e32 v110, v110
	v_rcp_f32_e32 v111, v111
	v_rcp_f32_e32 v107, v107
	v_rcp_f32_e32 v104, v104
	v_rcp_f32_e32 v105, v105
	v_rcp_f32_e32 v106, v106
	v_mul_f32_e32 v100, 0xbfb8aa3b, v100
	v_mul_f32_e32 v101, 0xbfb8aa3b, v101
	v_mul_f32_e32 v102, 0xbfb8aa3b, v102
	v_mul_f32_e32 v103, 0xbfb8aa3b, v103
	v_mul_f32_e32 v99, 0xbfb8aa3b, v99
	v_mul_f32_e32 v96, 0xbfb8aa3b, v96
	v_mul_f32_e32 v97, 0xbfb8aa3b, v97
	v_mul_f32_e32 v98, 0xbfb8aa3b, v98
	v_exp_f32_e32 v100, v100
	v_exp_f32_e32 v101, v101
	v_exp_f32_e32 v102, v102
	v_exp_f32_e32 v103, v103
	v_exp_f32_e32 v99, v99
	v_exp_f32_e32 v96, v96
	v_exp_f32_e32 v97, v97
	v_exp_f32_e32 v98, v98
	v_add_f32_e32 v100, 1.0, v100
	v_add_f32_e32 v101, 1.0, v101
	v_add_f32_e32 v102, 1.0, v102
	v_add_f32_e32 v103, 1.0, v103
	v_add_f32_e32 v99, 1.0, v99
	v_add_f32_e32 v96, 1.0, v96
	v_add_f32_e32 v97, 1.0, v97
	v_add_f32_e32 v98, 1.0, v98
	v_rcp_f32_e32 v100, v100
	v_rcp_f32_e32 v101, v101
	v_rcp_f32_e32 v102, v102
	v_rcp_f32_e32 v103, v103
	v_rcp_f32_e32 v99, v99
	v_rcp_f32_e32 v96, v96
	v_rcp_f32_e32 v97, v97
	v_rcp_f32_e32 v98, v98
	v_mul_f32_e32 v92, 0xbfb8aa3b, v92
	v_mul_f32_e32 v93, 0xbfb8aa3b, v93
	v_mul_f32_e32 v94, 0xbfb8aa3b, v94
	v_mul_f32_e32 v95, 0xbfb8aa3b, v95
	v_mul_f32_e32 v91, 0xbfb8aa3b, v91
	v_mul_f32_e32 v88, 0xbfb8aa3b, v88
	v_mul_f32_e32 v89, 0xbfb8aa3b, v89
	v_mul_f32_e32 v90, 0xbfb8aa3b, v90
	v_exp_f32_e32 v92, v92
	v_exp_f32_e32 v93, v93
	v_exp_f32_e32 v94, v94
	v_exp_f32_e32 v95, v95
	v_exp_f32_e32 v91, v91
	v_exp_f32_e32 v88, v88
	v_exp_f32_e32 v89, v89
	v_exp_f32_e32 v90, v90
	v_add_f32_e32 v92, 1.0, v92
	v_add_f32_e32 v93, 1.0, v93
	v_add_f32_e32 v94, 1.0, v94
	v_add_f32_e32 v95, 1.0, v95
	v_add_f32_e32 v91, 1.0, v91
	v_add_f32_e32 v88, 1.0, v88
	v_add_f32_e32 v89, 1.0, v89
	v_add_f32_e32 v90, 1.0, v90
	s_waitcnt vmcnt(1)
	v_lshlrev_b32_e32 v120, 16, v124
	v_and_b32_e32 v121, 0xffff0000, v124
	v_lshlrev_b32_e32 v122, 16, v125
	v_and_b32_e32 v123, 0xffff0000, v125
	v_lshlrev_b32_e32 v124, 16, v126
	v_and_b32_e32 v125, 0xffff0000, v126
	v_lshlrev_b32_e32 v126, 16, v127
	v_and_b32_e32 v127, 0xffff0000, v127
	v_mul_f32_e32 v116, v116, v120
	v_mul_f32_e32 v117, v117, v121
	v_mul_f32_e32 v118, v118, v122
	v_mul_f32_e32 v119, v119, v123
	v_mul_f32_e32 v120, v136, v124
	v_mul_f32_e32 v121, v154, v125
	v_mul_f32_e32 v122, v114, v126
	v_mul_f32_e32 v123, v115, v127
	v_cvt_pk_bf16_f32 v114, v116, v117
	v_cvt_pk_bf16_f32 v115, v118, v119
	v_cvt_pk_bf16_f32 v116, v120, v121
	v_cvt_pk_bf16_f32 v117, v122, v123
	global_load_dwordx4 v[118:121], v[152:153], off
	v_rcp_f32_e32 v92, v92
	global_store_dwordx4 v[112:113], v[114:117], off offset:256
	v_rcp_f32_e32 v93, v93
	v_rcp_f32_e32 v94, v94
	v_rcp_f32_e32 v95, v95
	v_rcp_f32_e32 v91, v91
	v_rcp_f32_e32 v88, v88
	v_rcp_f32_e32 v89, v89
	v_rcp_f32_e32 v90, v90
	v_mul_f32_e32 v84, 0xbfb8aa3b, v84
	v_mul_f32_e32 v85, 0xbfb8aa3b, v85
	v_mul_f32_e32 v86, 0xbfb8aa3b, v86
	v_mul_f32_e32 v87, 0xbfb8aa3b, v87
	v_mul_f32_e32 v83, 0xbfb8aa3b, v83
	v_mul_f32_e32 v80, 0xbfb8aa3b, v80
	v_mul_f32_e32 v81, 0xbfb8aa3b, v81
	v_mul_f32_e32 v82, 0xbfb8aa3b, v82
	v_exp_f32_e32 v84, v84
	v_exp_f32_e32 v85, v85
	v_exp_f32_e32 v86, v86
	v_exp_f32_e32 v87, v87
	v_exp_f32_e32 v83, v83
	v_exp_f32_e32 v80, v80
	v_exp_f32_e32 v81, v81
	v_exp_f32_e32 v82, v82
	v_add_f32_e32 v84, 1.0, v84
	v_add_f32_e32 v85, 1.0, v85
	v_add_f32_e32 v86, 1.0, v86
	v_add_f32_e32 v87, 1.0, v87
	v_add_f32_e32 v83, 1.0, v83
	v_add_f32_e32 v80, 1.0, v80
	v_add_f32_e32 v81, 1.0, v81
	v_add_f32_e32 v82, 1.0, v82
	v_rcp_f32_e32 v84, v84
	v_rcp_f32_e32 v85, v85
	v_rcp_f32_e32 v86, v86
	v_rcp_f32_e32 v87, v87
	v_rcp_f32_e32 v83, v83
	v_rcp_f32_e32 v80, v80
	v_rcp_f32_e32 v81, v81
	v_rcp_f32_e32 v82, v82
	v_mul_f32_e32 v76, 0xbfb8aa3b, v76
	v_mul_f32_e32 v77, 0xbfb8aa3b, v77
	v_mul_f32_e32 v78, 0xbfb8aa3b, v78
	v_mul_f32_e32 v79, 0xbfb8aa3b, v79
	v_mul_f32_e32 v75, 0xbfb8aa3b, v75
	v_mul_f32_e32 v72, 0xbfb8aa3b, v72
	v_mul_f32_e32 v73, 0xbfb8aa3b, v73
	v_mul_f32_e32 v74, 0xbfb8aa3b, v74
	v_exp_f32_e32 v76, v76
	v_exp_f32_e32 v77, v77
	v_exp_f32_e32 v78, v78
	v_exp_f32_e32 v79, v79
	v_exp_f32_e32 v75, v75
	v_exp_f32_e32 v72, v72
	v_exp_f32_e32 v73, v73
	v_exp_f32_e32 v74, v74
	v_add_f32_e32 v76, 1.0, v76
	v_add_f32_e32 v77, 1.0, v77
	v_add_f32_e32 v78, 1.0, v78
	v_add_f32_e32 v79, 1.0, v79
	v_add_f32_e32 v75, 1.0, v75
	v_add_f32_e32 v72, 1.0, v72
	v_add_f32_e32 v73, 1.0, v73
	v_add_f32_e32 v74, 1.0, v74
	v_rcp_f32_e32 v76, v76
	v_rcp_f32_e32 v77, v77
	v_rcp_f32_e32 v78, v78
	v_rcp_f32_e32 v79, v79
	v_rcp_f32_e32 v75, v75
	v_rcp_f32_e32 v72, v72
	v_rcp_f32_e32 v73, v73
	v_rcp_f32_e32 v74, v74
	v_mul_f32_e32 v68, 0xbfb8aa3b, v68
	v_mul_f32_e32 v69, 0xbfb8aa3b, v69
	v_mul_f32_e32 v70, 0xbfb8aa3b, v70
	v_mul_f32_e32 v71, 0xbfb8aa3b, v71
	v_mul_f32_e32 v67, 0xbfb8aa3b, v67
	v_mul_f32_e32 v64, 0xbfb8aa3b, v64
	s_waitcnt vmcnt(1)
	v_lshlrev_b32_e32 v114, 16, v118
	v_and_b32_e32 v115, 0xffff0000, v118
	v_lshlrev_b32_e32 v116, 16, v119
	v_and_b32_e32 v117, 0xffff0000, v119
	v_lshlrev_b32_e32 v118, 16, v120
	v_and_b32_e32 v119, 0xffff0000, v120
	v_lshlrev_b32_e32 v120, 16, v121
	v_and_b32_e32 v121, 0xffff0000, v121
	v_mul_f32_e32 v108, v108, v114
	v_mul_f32_e32 v109, v109, v115
	v_mul_f32_e32 v110, v110, v116
	v_mul_f32_e32 v111, v111, v117
	v_mul_f32_e32 v107, v107, v121
	v_mul_f32_e32 v114, v104, v118
	v_mul_f32_e32 v115, v105, v119
	v_mul_f32_e32 v116, v106, v120
	v_cvt_pk_bf16_f32 v104, v108, v109
	v_cvt_pk_bf16_f32 v105, v110, v111
	v_cvt_pk_bf16_f32 v106, v114, v115
	v_cvt_pk_bf16_f32 v107, v116, v107
	global_load_dwordx4 v[108:111], v[152:153], off offset:256
	v_add_co_u32_e32 v114, vcc, s47, v112
	v_mul_f32_e32 v65, 0xbfb8aa3b, v65
	s_nop 0
	v_addc_co_u32_e32 v115, vcc, 0, v113, vcc
	v_add_co_u32_e32 v116, vcc, s41, v146
	global_store_dwordx4 v[114:115], v[104:107], off
	s_nop 0
	v_addc_co_u32_e32 v117, vcc, 0, v147, vcc
	v_mul_f32_e32 v66, 0xbfb8aa3b, v66
	v_exp_f32_e32 v68, v68
	v_exp_f32_e32 v69, v69
	v_exp_f32_e32 v70, v70
	v_exp_f32_e32 v71, v71
	v_exp_f32_e32 v67, v67
	v_exp_f32_e32 v64, v64
	v_exp_f32_e32 v65, v65
	v_exp_f32_e32 v66, v66
	v_add_f32_e32 v68, 1.0, v68
	v_add_f32_e32 v69, 1.0, v69
	v_add_f32_e32 v70, 1.0, v70
	v_add_f32_e32 v71, 1.0, v71
	v_add_f32_e32 v67, 1.0, v67
	v_add_f32_e32 v64, 1.0, v64
	v_add_f32_e32 v65, 1.0, v65
	v_add_f32_e32 v66, 1.0, v66
	v_rcp_f32_e32 v68, v68
	v_rcp_f32_e32 v69, v69
	v_rcp_f32_e32 v70, v70
	v_rcp_f32_e32 v71, v71
	v_rcp_f32_e32 v67, v67
	v_rcp_f32_e32 v64, v64
	v_rcp_f32_e32 v65, v65
	v_rcp_f32_e32 v66, v66
	v_mul_f32_e32 v60, 0xbfb8aa3b, v60
	v_mul_f32_e32 v61, 0xbfb8aa3b, v61
	v_mul_f32_e32 v62, 0xbfb8aa3b, v62
	v_mul_f32_e32 v63, 0xbfb8aa3b, v63
	v_mul_f32_e32 v59, 0xbfb8aa3b, v59
	v_mul_f32_e32 v56, 0xbfb8aa3b, v56
	v_mul_f32_e32 v57, 0xbfb8aa3b, v57
	v_mul_f32_e32 v58, 0xbfb8aa3b, v58
	v_exp_f32_e32 v60, v60
	v_exp_f32_e32 v61, v61
	v_exp_f32_e32 v62, v62
	v_exp_f32_e32 v63, v63
	v_exp_f32_e32 v59, v59
	v_exp_f32_e32 v56, v56
	v_exp_f32_e32 v57, v57
	v_exp_f32_e32 v58, v58
	v_add_f32_e32 v60, 1.0, v60
	v_add_f32_e32 v61, 1.0, v61
	v_add_f32_e32 v62, 1.0, v62
	v_add_f32_e32 v63, 1.0, v63
	v_add_f32_e32 v59, 1.0, v59
	v_add_f32_e32 v56, 1.0, v56
	v_add_f32_e32 v57, 1.0, v57
	v_add_f32_e32 v58, 1.0, v58
	v_rcp_f32_e32 v60, v60
	v_rcp_f32_e32 v61, v61
	v_rcp_f32_e32 v62, v62
	v_rcp_f32_e32 v63, v63
	v_rcp_f32_e32 v59, v59
	v_rcp_f32_e32 v56, v56
	v_rcp_f32_e32 v57, v57
	v_rcp_f32_e32 v58, v58
	v_mul_f32_e32 v52, 0xbfb8aa3b, v52
	v_mul_f32_e32 v53, 0xbfb8aa3b, v53
	v_mul_f32_e32 v54, 0xbfb8aa3b, v54
	v_mul_f32_e32 v55, 0xbfb8aa3b, v55
	v_mul_f32_e32 v51, 0xbfb8aa3b, v51
	v_mul_f32_e32 v48, 0xbfb8aa3b, v48
	v_mul_f32_e32 v49, 0xbfb8aa3b, v49
	v_mul_f32_e32 v50, 0xbfb8aa3b, v50
	v_exp_f32_e32 v52, v52
	v_exp_f32_e32 v53, v53
	v_exp_f32_e32 v54, v54
	v_exp_f32_e32 v55, v55
	s_waitcnt vmcnt(1)
	v_lshlrev_b32_e32 v104, 16, v108
	v_and_b32_e32 v105, 0xffff0000, v108
	v_lshlrev_b32_e32 v106, 16, v109
	v_and_b32_e32 v107, 0xffff0000, v109
	v_lshlrev_b32_e32 v108, 16, v110
	v_and_b32_e32 v109, 0xffff0000, v110
	v_lshlrev_b32_e32 v110, 16, v111
	v_and_b32_e32 v111, 0xffff0000, v111
	v_mul_f32_e32 v100, v100, v104
	v_mul_f32_e32 v101, v101, v105
	v_mul_f32_e32 v102, v102, v106
	v_mul_f32_e32 v103, v103, v107
	v_mul_f32_e32 v99, v99, v111
	v_mul_f32_e32 v104, v96, v108
	v_mul_f32_e32 v105, v97, v109
	v_mul_f32_e32 v106, v98, v110
	v_cvt_pk_bf16_f32 v96, v100, v101
	v_cvt_pk_bf16_f32 v97, v102, v103
	v_cvt_pk_bf16_f32 v98, v104, v105
	v_cvt_pk_bf16_f32 v99, v106, v99
	global_load_dwordx4 v[100:103], v[116:117], off
	v_exp_f32_e32 v51, v51
	global_store_dwordx4 v[114:115], v[96:99], off offset:256
	v_exp_f32_e32 v48, v48
	v_exp_f32_e32 v49, v49
	v_exp_f32_e32 v50, v50
	v_add_f32_e32 v52, 1.0, v52
	v_add_f32_e32 v53, 1.0, v53
	v_add_f32_e32 v54, 1.0, v54
	v_add_f32_e32 v55, 1.0, v55
	v_add_f32_e32 v51, 1.0, v51
	v_add_f32_e32 v48, 1.0, v48
	v_add_f32_e32 v49, 1.0, v49
	v_add_f32_e32 v50, 1.0, v50
	v_rcp_f32_e32 v52, v52
	v_rcp_f32_e32 v53, v53
	v_rcp_f32_e32 v54, v54
	v_rcp_f32_e32 v55, v55
	v_rcp_f32_e32 v51, v51
	v_rcp_f32_e32 v48, v48
	v_rcp_f32_e32 v49, v49
	v_rcp_f32_e32 v50, v50
	v_mul_f32_e32 v44, 0xbfb8aa3b, v44
	v_mul_f32_e32 v45, 0xbfb8aa3b, v45
	v_mul_f32_e32 v46, 0xbfb8aa3b, v46
	v_mul_f32_e32 v47, 0xbfb8aa3b, v47
	v_mul_f32_e32 v43, 0xbfb8aa3b, v43
	v_mul_f32_e32 v40, 0xbfb8aa3b, v40
	v_mul_f32_e32 v41, 0xbfb8aa3b, v41
	v_mul_f32_e32 v42, 0xbfb8aa3b, v42
	v_exp_f32_e32 v44, v44
	v_exp_f32_e32 v45, v45
	v_exp_f32_e32 v46, v46
	v_exp_f32_e32 v47, v47
	v_exp_f32_e32 v43, v43
	v_exp_f32_e32 v40, v40
	v_exp_f32_e32 v41, v41
	v_exp_f32_e32 v42, v42
	v_add_f32_e32 v44, 1.0, v44
	v_add_f32_e32 v45, 1.0, v45
	v_add_f32_e32 v46, 1.0, v46
	v_add_f32_e32 v47, 1.0, v47
	v_add_f32_e32 v43, 1.0, v43
	v_add_f32_e32 v40, 1.0, v40
	v_add_f32_e32 v41, 1.0, v41
	v_add_f32_e32 v42, 1.0, v42
	v_rcp_f32_e32 v44, v44
	v_rcp_f32_e32 v45, v45
	v_rcp_f32_e32 v46, v46
	v_rcp_f32_e32 v47, v47
	v_rcp_f32_e32 v43, v43
	v_rcp_f32_e32 v40, v40
	v_rcp_f32_e32 v41, v41
	v_rcp_f32_e32 v42, v42
	v_mul_f32_e32 v36, 0xbfb8aa3b, v36
	v_mul_f32_e32 v37, 0xbfb8aa3b, v37
	v_mul_f32_e32 v38, 0xbfb8aa3b, v38
	v_mul_f32_e32 v39, 0xbfb8aa3b, v39
	v_mul_f32_e32 v35, 0xbfb8aa3b, v35
	v_mul_f32_e32 v32, 0xbfb8aa3b, v32
	v_mul_f32_e32 v33, 0xbfb8aa3b, v33
	v_mul_f32_e32 v34, 0xbfb8aa3b, v34
	v_exp_f32_e32 v36, v36
	v_exp_f32_e32 v37, v37
	v_exp_f32_e32 v38, v38
	v_exp_f32_e32 v39, v39
	v_exp_f32_e32 v35, v35
	v_exp_f32_e32 v32, v32
	v_exp_f32_e32 v33, v33
	v_exp_f32_e32 v34, v34
	v_add_f32_e32 v36, 1.0, v36
	v_add_f32_e32 v37, 1.0, v37
	v_add_f32_e32 v38, 1.0, v38
	v_add_f32_e32 v39, 1.0, v39
	v_add_f32_e32 v35, 1.0, v35
	v_add_f32_e32 v32, 1.0, v32
	v_add_f32_e32 v33, 1.0, v33
	v_add_f32_e32 v34, 1.0, v34
	v_rcp_f32_e32 v36, v36
	v_rcp_f32_e32 v37, v37
	s_waitcnt vmcnt(1)
	v_lshlrev_b32_e32 v96, 16, v100
	v_and_b32_e32 v97, 0xffff0000, v100
	v_lshlrev_b32_e32 v98, 16, v101
	v_and_b32_e32 v99, 0xffff0000, v101
	v_lshlrev_b32_e32 v100, 16, v102
	v_and_b32_e32 v101, 0xffff0000, v102
	v_lshlrev_b32_e32 v102, 16, v103
	v_and_b32_e32 v103, 0xffff0000, v103
	v_mul_f32_e32 v92, v92, v96
	v_mul_f32_e32 v93, v93, v97
	v_mul_f32_e32 v94, v94, v98
	v_mul_f32_e32 v95, v95, v99
	v_mul_f32_e32 v91, v91, v103
	v_mul_f32_e32 v96, v88, v100
	v_mul_f32_e32 v97, v89, v101
	v_mul_f32_e32 v98, v90, v102
	v_cvt_pk_bf16_f32 v88, v92, v93
	v_cvt_pk_bf16_f32 v89, v94, v95
	v_cvt_pk_bf16_f32 v90, v96, v97
	v_cvt_pk_bf16_f32 v91, v98, v91
	global_load_dwordx4 v[92:95], v[116:117], off offset:256
	v_add_co_u32_e32 v96, vcc, s41, v112
	v_rcp_f32_e32 v38, v38
	s_nop 0
	v_addc_co_u32_e32 v97, vcc, 0, v113, vcc
	v_add_co_u32_e32 v98, vcc, s46, v146
	global_store_dwordx4 v[96:97], v[88:91], off
	s_nop 0
	v_addc_co_u32_e32 v99, vcc, 0, v147, vcc
	v_rcp_f32_e32 v39, v39
	v_rcp_f32_e32 v35, v35
	v_rcp_f32_e32 v32, v32
	v_rcp_f32_e32 v33, v33
	v_rcp_f32_e32 v34, v34
	v_mul_f32_e32 v28, 0xbfb8aa3b, v28
	v_mul_f32_e32 v29, 0xbfb8aa3b, v29
	v_mul_f32_e32 v30, 0xbfb8aa3b, v30
	v_mul_f32_e32 v31, 0xbfb8aa3b, v31
	v_mul_f32_e32 v27, 0xbfb8aa3b, v27
	v_mul_f32_e32 v24, 0xbfb8aa3b, v24
	v_mul_f32_e32 v25, 0xbfb8aa3b, v25
	v_mul_f32_e32 v26, 0xbfb8aa3b, v26
	v_exp_f32_e32 v28, v28
	v_exp_f32_e32 v29, v29
	v_exp_f32_e32 v30, v30
	v_exp_f32_e32 v31, v31
	v_exp_f32_e32 v27, v27
	v_exp_f32_e32 v24, v24
	v_exp_f32_e32 v25, v25
	v_exp_f32_e32 v26, v26
	v_add_f32_e32 v28, 1.0, v28
	v_add_f32_e32 v29, 1.0, v29
	v_add_f32_e32 v30, 1.0, v30
	v_add_f32_e32 v31, 1.0, v31
	v_add_f32_e32 v27, 1.0, v27
	v_add_f32_e32 v24, 1.0, v24
	v_add_f32_e32 v25, 1.0, v25
	v_add_f32_e32 v26, 1.0, v26
	v_rcp_f32_e32 v28, v28
	v_rcp_f32_e32 v29, v29
	v_rcp_f32_e32 v30, v30
	v_rcp_f32_e32 v31, v31
	v_rcp_f32_e32 v27, v27
	v_rcp_f32_e32 v24, v24
	v_rcp_f32_e32 v25, v25
	v_rcp_f32_e32 v26, v26
	v_mul_f32_e32 v20, 0xbfb8aa3b, v20
	v_mul_f32_e32 v21, 0xbfb8aa3b, v21
	v_mul_f32_e32 v22, 0xbfb8aa3b, v22
	v_mul_f32_e32 v23, 0xbfb8aa3b, v23
	v_mul_f32_e32 v19, 0xbfb8aa3b, v19
	v_mul_f32_e32 v16, 0xbfb8aa3b, v16
	v_mul_f32_e32 v17, 0xbfb8aa3b, v17
	v_mul_f32_e32 v18, 0xbfb8aa3b, v18
	v_exp_f32_e32 v20, v20
	v_exp_f32_e32 v21, v21
	v_exp_f32_e32 v22, v22
	v_exp_f32_e32 v23, v23
	v_exp_f32_e32 v19, v19
	v_exp_f32_e32 v16, v16
	v_exp_f32_e32 v17, v17
	v_exp_f32_e32 v18, v18
	v_add_f32_e32 v20, 1.0, v20
	v_add_f32_e32 v21, 1.0, v21
	v_add_f32_e32 v22, 1.0, v22
	v_add_f32_e32 v23, 1.0, v23
	v_add_f32_e32 v19, 1.0, v19
	v_add_f32_e32 v16, 1.0, v16
	v_add_f32_e32 v17, 1.0, v17
	v_add_f32_e32 v18, 1.0, v18
	v_rcp_f32_e32 v20, v20
	v_rcp_f32_e32 v21, v21
	v_rcp_f32_e32 v22, v22
	v_rcp_f32_e32 v23, v23
	v_rcp_f32_e32 v19, v19
	v_rcp_f32_e32 v16, v16
	v_rcp_f32_e32 v17, v17
	v_rcp_f32_e32 v18, v18
	s_waitcnt vmcnt(1)
	v_lshlrev_b32_e32 v88, 16, v92
	v_and_b32_e32 v89, 0xffff0000, v92
	v_lshlrev_b32_e32 v90, 16, v93
	v_and_b32_e32 v91, 0xffff0000, v93
	v_lshlrev_b32_e32 v92, 16, v94
	v_and_b32_e32 v93, 0xffff0000, v94
	v_lshlrev_b32_e32 v94, 16, v95
	v_and_b32_e32 v95, 0xffff0000, v95
	v_mul_f32_e32 v84, v84, v88
	v_mul_f32_e32 v85, v85, v89
	v_mul_f32_e32 v86, v86, v90
	v_mul_f32_e32 v87, v87, v91
	v_mul_f32_e32 v83, v83, v95
	v_mul_f32_e32 v88, v80, v92
	v_mul_f32_e32 v89, v81, v93
	v_mul_f32_e32 v90, v82, v94
	v_cvt_pk_bf16_f32 v80, v84, v85
	v_cvt_pk_bf16_f32 v81, v86, v87
	v_cvt_pk_bf16_f32 v82, v88, v89
	v_cvt_pk_bf16_f32 v83, v90, v83
	global_load_dwordx4 v[84:87], v[98:99], off
	v_mul_f32_e32 v12, 0xbfb8aa3b, v12
	global_store_dwordx4 v[96:97], v[80:83], off offset:256
	v_mul_f32_e32 v13, 0xbfb8aa3b, v13
	v_mul_f32_e32 v14, 0xbfb8aa3b, v14
	v_mul_f32_e32 v15, 0xbfb8aa3b, v15
	v_mul_f32_e32 v11, 0xbfb8aa3b, v11
	v_mul_f32_e32 v8, 0xbfb8aa3b, v8
	v_mul_f32_e32 v9, 0xbfb8aa3b, v9
	v_mul_f32_e32 v10, 0xbfb8aa3b, v10
	v_exp_f32_e32 v12, v12
	v_exp_f32_e32 v13, v13
	v_exp_f32_e32 v14, v14
	v_exp_f32_e32 v15, v15
	v_exp_f32_e32 v11, v11
	v_exp_f32_e32 v8, v8
	v_exp_f32_e32 v9, v9
	v_exp_f32_e32 v10, v10
	v_add_f32_e32 v12, 1.0, v12
	v_add_f32_e32 v13, 1.0, v13
	v_add_f32_e32 v14, 1.0, v14
	v_add_f32_e32 v15, 1.0, v15
	v_add_f32_e32 v11, 1.0, v11
	v_add_f32_e32 v8, 1.0, v8
	v_add_f32_e32 v9, 1.0, v9
	v_add_f32_e32 v10, 1.0, v10
	v_rcp_f32_e32 v12, v12
	v_rcp_f32_e32 v13, v13
	v_rcp_f32_e32 v14, v14
	v_rcp_f32_e32 v15, v15
	v_rcp_f32_e32 v11, v11
	v_rcp_f32_e32 v8, v8
	v_rcp_f32_e32 v9, v9
	v_rcp_f32_e32 v10, v10
	v_mul_f32_e32 v3, 0xbfb8aa3b, v3
	v_mul_f32_e32 v4, 0xbfb8aa3b, v4
	v_mul_f32_e32 v5, 0xbfb8aa3b, v5
	v_mul_f32_e32 v6, 0xbfb8aa3b, v6
	v_mul_f32_e32 v7, 0xbfb8aa3b, v7
	v_mul_f32_e32 v0, 0xbfb8aa3b, v0
	v_mul_f32_e32 v1, 0xbfb8aa3b, v1
	v_mul_f32_e32 v2, 0xbfb8aa3b, v2
	v_exp_f32_e32 v3, v3
	v_exp_f32_e32 v4, v4
	v_exp_f32_e32 v5, v5
	v_exp_f32_e32 v6, v6
	v_exp_f32_e32 v7, v7
	v_exp_f32_e32 v0, v0
	v_exp_f32_e32 v1, v1
	v_exp_f32_e32 v2, v2
	v_add_f32_e32 v3, 1.0, v3
	v_add_f32_e32 v4, 1.0, v4
	v_add_f32_e32 v5, 1.0, v5
	v_add_f32_e32 v6, 1.0, v6
	v_add_f32_e32 v7, 1.0, v7
	v_add_f32_e32 v0, 1.0, v0
	v_add_f32_e32 v1, 1.0, v1
	v_add_f32_e32 v2, 1.0, v2
	v_rcp_f32_e32 v3, v3
	v_rcp_f32_e32 v6, v6
	v_rcp_f32_e32 v7, v7
	v_rcp_f32_e32 v0, v0
	v_rcp_f32_e32 v1, v1
	v_rcp_f32_e32 v2, v2
	s_waitcnt vmcnt(1)
	v_lshlrev_b32_e32 v80, 16, v84
	v_and_b32_e32 v81, 0xffff0000, v84
	v_lshlrev_b32_e32 v82, 16, v85
	v_and_b32_e32 v83, 0xffff0000, v85
	v_lshlrev_b32_e32 v84, 16, v86
	v_and_b32_e32 v85, 0xffff0000, v86
	v_lshlrev_b32_e32 v86, 16, v87
	v_and_b32_e32 v87, 0xffff0000, v87
	v_mul_f32_e32 v76, v76, v80
	v_mul_f32_e32 v77, v77, v81
	v_mul_f32_e32 v78, v78, v82
	v_mul_f32_e32 v79, v79, v83
	v_mul_f32_e32 v75, v75, v87
	v_mul_f32_e32 v80, v72, v84
	v_mul_f32_e32 v81, v73, v85
	v_mul_f32_e32 v82, v74, v86
	v_cvt_pk_bf16_f32 v72, v76, v77
	v_cvt_pk_bf16_f32 v73, v78, v79
	v_cvt_pk_bf16_f32 v74, v80, v81
	v_cvt_pk_bf16_f32 v75, v82, v75
	global_load_dwordx4 v[76:79], v[98:99], off offset:256
	v_add_co_u32_e32 v80, vcc, s46, v112
	s_nop 1
	v_addc_co_u32_e32 v81, vcc, 0, v113, vcc
	v_add_co_u32_e32 v82, vcc, s50, v146
	global_store_dwordx4 v[80:81], v[72:75], off
	s_nop 0
	v_addc_co_u32_e32 v83, vcc, 0, v147, vcc
	s_waitcnt vmcnt(1)
	v_lshlrev_b32_e32 v72, 16, v76
	v_and_b32_e32 v73, 0xffff0000, v76
	v_lshlrev_b32_e32 v74, 16, v77
	v_and_b32_e32 v75, 0xffff0000, v77
	v_lshlrev_b32_e32 v76, 16, v78
	v_and_b32_e32 v77, 0xffff0000, v78
	v_lshlrev_b32_e32 v78, 16, v79
	v_and_b32_e32 v79, 0xffff0000, v79
	v_mul_f32_e32 v68, v68, v72
	v_mul_f32_e32 v69, v69, v73
	v_mul_f32_e32 v70, v70, v74
	v_mul_f32_e32 v71, v71, v75
	v_mul_f32_e32 v67, v67, v79
	v_mul_f32_e32 v72, v64, v76
	v_mul_f32_e32 v73, v65, v77
	v_mul_f32_e32 v74, v66, v78
	v_cvt_pk_bf16_f32 v64, v68, v69
	v_cvt_pk_bf16_f32 v65, v70, v71
	v_cvt_pk_bf16_f32 v66, v72, v73
	v_cvt_pk_bf16_f32 v67, v74, v67
	global_load_dwordx4 v[68:71], v[82:83], off
	s_nop 0
	global_store_dwordx4 v[80:81], v[64:67], off offset:256
	s_waitcnt vmcnt(1)
	s_nop 0
	v_lshlrev_b32_e32 v64, 16, v68
	v_and_b32_e32 v65, 0xffff0000, v68
	v_lshlrev_b32_e32 v66, 16, v69
	v_and_b32_e32 v67, 0xffff0000, v69
	v_lshlrev_b32_e32 v68, 16, v70
	v_and_b32_e32 v69, 0xffff0000, v70
	v_lshlrev_b32_e32 v70, 16, v71
	v_and_b32_e32 v71, 0xffff0000, v71
	v_mul_f32_e32 v60, v60, v64
	v_mul_f32_e32 v61, v61, v65
	v_mul_f32_e32 v62, v62, v66
	v_mul_f32_e32 v63, v63, v67
	v_mul_f32_e32 v59, v59, v71
	v_mul_f32_e32 v64, v56, v68
	v_mul_f32_e32 v65, v57, v69
	v_mul_f32_e32 v66, v58, v70
	v_cvt_pk_bf16_f32 v56, v60, v61
	v_cvt_pk_bf16_f32 v57, v62, v63
	v_cvt_pk_bf16_f32 v58, v64, v65
	v_cvt_pk_bf16_f32 v59, v66, v59
	global_load_dwordx4 v[60:63], v[82:83], off offset:256
	v_add_co_u32_e32 v64, vcc, s50, v112
	s_nop 1
	v_addc_co_u32_e32 v65, vcc, 0, v113, vcc
	v_add_co_u32_e32 v66, vcc, s51, v146
	global_store_dwordx4 v[64:65], v[56:59], off
	s_nop 0
	v_addc_co_u32_e32 v67, vcc, 0, v147, vcc
	s_waitcnt vmcnt(1)
	v_lshlrev_b32_e32 v56, 16, v60
	v_and_b32_e32 v57, 0xffff0000, v60
	v_lshlrev_b32_e32 v58, 16, v61
	v_and_b32_e32 v59, 0xffff0000, v61
	v_lshlrev_b32_e32 v60, 16, v62
	v_and_b32_e32 v61, 0xffff0000, v62
	v_lshlrev_b32_e32 v62, 16, v63
	v_and_b32_e32 v63, 0xffff0000, v63
	v_mul_f32_e32 v52, v52, v56
	v_mul_f32_e32 v53, v53, v57
	v_mul_f32_e32 v54, v54, v58
	v_mul_f32_e32 v55, v55, v59
	v_mul_f32_e32 v51, v51, v63
	v_mul_f32_e32 v56, v48, v60
	v_mul_f32_e32 v57, v49, v61
	v_mul_f32_e32 v58, v50, v62
	v_cvt_pk_bf16_f32 v48, v52, v53
	v_cvt_pk_bf16_f32 v49, v54, v55
	v_cvt_pk_bf16_f32 v50, v56, v57
	v_cvt_pk_bf16_f32 v51, v58, v51
	global_load_dwordx4 v[52:55], v[66:67], off
	s_nop 0
	global_store_dwordx4 v[64:65], v[48:51], off offset:256
	s_waitcnt vmcnt(1)
	s_nop 0
	v_lshlrev_b32_e32 v48, 16, v52
	v_and_b32_e32 v49, 0xffff0000, v52
	v_lshlrev_b32_e32 v50, 16, v53
	v_and_b32_e32 v51, 0xffff0000, v53
	v_lshlrev_b32_e32 v52, 16, v54
	v_and_b32_e32 v53, 0xffff0000, v54
	v_lshlrev_b32_e32 v54, 16, v55
	v_and_b32_e32 v55, 0xffff0000, v55
	v_mul_f32_e32 v44, v44, v48
	v_mul_f32_e32 v45, v45, v49
	v_mul_f32_e32 v46, v46, v50
	v_mul_f32_e32 v47, v47, v51
	v_mul_f32_e32 v43, v43, v55
	v_mul_f32_e32 v48, v40, v52
	v_mul_f32_e32 v49, v41, v53
	v_mul_f32_e32 v50, v42, v54
	v_cvt_pk_bf16_f32 v40, v44, v45
	v_cvt_pk_bf16_f32 v41, v46, v47
	v_cvt_pk_bf16_f32 v42, v48, v49
	v_cvt_pk_bf16_f32 v43, v50, v43
	global_load_dwordx4 v[44:47], v[66:67], off offset:256
	v_add_co_u32_e32 v48, vcc, s51, v112
	s_nop 1
	v_addc_co_u32_e32 v49, vcc, 0, v113, vcc
	v_add_co_u32_e32 v50, vcc, s52, v146
	global_store_dwordx4 v[48:49], v[40:43], off
	s_nop 0
	v_addc_co_u32_e32 v51, vcc, 0, v147, vcc
	s_waitcnt vmcnt(1)
	v_lshlrev_b32_e32 v40, 16, v44
	v_and_b32_e32 v41, 0xffff0000, v44
	v_lshlrev_b32_e32 v42, 16, v45
	v_and_b32_e32 v43, 0xffff0000, v45
	v_lshlrev_b32_e32 v44, 16, v46
	v_and_b32_e32 v45, 0xffff0000, v46
	v_lshlrev_b32_e32 v46, 16, v47
	v_and_b32_e32 v47, 0xffff0000, v47
	v_mul_f32_e32 v36, v36, v40
	v_mul_f32_e32 v37, v37, v41
	v_mul_f32_e32 v38, v38, v42
	v_mul_f32_e32 v39, v39, v43
	v_mul_f32_e32 v35, v35, v47
	v_mul_f32_e32 v40, v32, v44
	v_mul_f32_e32 v41, v33, v45
	v_mul_f32_e32 v42, v34, v46
	v_cvt_pk_bf16_f32 v32, v36, v37
	v_cvt_pk_bf16_f32 v33, v38, v39
	v_cvt_pk_bf16_f32 v34, v40, v41
	v_cvt_pk_bf16_f32 v35, v42, v35
	global_load_dwordx4 v[36:39], v[50:51], off
	s_nop 0
	global_store_dwordx4 v[48:49], v[32:35], off offset:256
	s_waitcnt vmcnt(1)
	s_nop 0
	v_lshlrev_b32_e32 v32, 16, v36
	v_and_b32_e32 v33, 0xffff0000, v36
	v_lshlrev_b32_e32 v34, 16, v37
	v_and_b32_e32 v35, 0xffff0000, v37
	v_lshlrev_b32_e32 v36, 16, v38
	v_and_b32_e32 v37, 0xffff0000, v38
	v_lshlrev_b32_e32 v38, 16, v39
	v_and_b32_e32 v39, 0xffff0000, v39
	v_mul_f32_e32 v28, v28, v32
	v_mul_f32_e32 v29, v29, v33
	v_mul_f32_e32 v30, v30, v34
	v_mul_f32_e32 v31, v31, v35
	v_mul_f32_e32 v27, v27, v39
	v_mul_f32_e32 v32, v24, v36
	v_mul_f32_e32 v33, v25, v37
	v_mul_f32_e32 v34, v26, v38
	v_cvt_pk_bf16_f32 v24, v28, v29
	v_cvt_pk_bf16_f32 v25, v30, v31
	v_cvt_pk_bf16_f32 v26, v32, v33
	v_cvt_pk_bf16_f32 v27, v34, v27
	global_load_dwordx4 v[28:31], v[50:51], off offset:256
	v_add_co_u32_e32 v32, vcc, s52, v112
	s_nop 1
	v_addc_co_u32_e32 v33, vcc, 0, v113, vcc
	v_add_co_u32_e32 v34, vcc, s53, v146
	global_store_dwordx4 v[32:33], v[24:27], off
	s_nop 0
	v_addc_co_u32_e32 v35, vcc, 0, v147, vcc
	s_andn2_b64 vcc, exec, s[0:1]
	s_waitcnt vmcnt(1)
	v_lshlrev_b32_e32 v24, 16, v28
	v_and_b32_e32 v25, 0xffff0000, v28
	v_lshlrev_b32_e32 v26, 16, v29
	v_and_b32_e32 v27, 0xffff0000, v29
	v_lshlrev_b32_e32 v28, 16, v30
	v_and_b32_e32 v29, 0xffff0000, v30
	v_lshlrev_b32_e32 v30, 16, v31
	v_and_b32_e32 v31, 0xffff0000, v31
	v_mul_f32_e32 v20, v20, v24
	v_mul_f32_e32 v21, v21, v25
	v_mul_f32_e32 v22, v22, v26
	v_mul_f32_e32 v23, v23, v27
	v_mul_f32_e32 v19, v19, v31
	v_mul_f32_e32 v24, v16, v28
	v_mul_f32_e32 v25, v17, v29
	v_mul_f32_e32 v26, v18, v30
	v_cvt_pk_bf16_f32 v16, v20, v21
	v_cvt_pk_bf16_f32 v17, v22, v23
	v_cvt_pk_bf16_f32 v18, v24, v25
	v_cvt_pk_bf16_f32 v19, v26, v19
	global_load_dwordx4 v[20:23], v[34:35], off
	s_nop 0
	global_store_dwordx4 v[32:33], v[16:19], off offset:256
	s_waitcnt vmcnt(1)
	s_nop 0
	v_lshlrev_b32_e32 v16, 16, v20
	v_and_b32_e32 v17, 0xffff0000, v20
	v_lshlrev_b32_e32 v18, 16, v21
	v_and_b32_e32 v19, 0xffff0000, v21
	v_lshlrev_b32_e32 v20, 16, v22
	v_and_b32_e32 v21, 0xffff0000, v22
	v_lshlrev_b32_e32 v22, 16, v23
	v_and_b32_e32 v23, 0xffff0000, v23
	v_mul_f32_e32 v12, v12, v16
	v_mul_f32_e32 v13, v13, v17
	v_mul_f32_e32 v14, v14, v18
	v_mul_f32_e32 v15, v15, v19
	v_mul_f32_e32 v11, v11, v23
	v_mul_f32_e32 v16, v8, v20
	v_mul_f32_e32 v17, v9, v21
	v_mul_f32_e32 v18, v10, v22
	v_cvt_pk_bf16_f32 v8, v12, v13
	v_cvt_pk_bf16_f32 v9, v14, v15
	v_cvt_pk_bf16_f32 v10, v16, v17
	v_cvt_pk_bf16_f32 v11, v18, v11
	global_load_dwordx4 v[12:15], v[34:35], off offset:256
	v_rcp_f32_e32 v16, v4
	v_rcp_f32_e32 v17, v5
	v_add_co_u32_e64 v4, s[0:1], s53, v112
	s_nop 1
	v_addc_co_u32_e64 v5, s[0:1], 0, v113, s[0:1]
	global_store_dwordx4 v[4:5], v[8:11], off
	s_mov_b64 s[0:1], -1
	s_waitcnt vmcnt(1)
	v_lshlrev_b32_e32 v8, 16, v12
	v_and_b32_e32 v9, 0xffff0000, v12
	v_lshlrev_b32_e32 v10, 16, v13
	v_and_b32_e32 v11, 0xffff0000, v13
	v_lshlrev_b32_e32 v12, 16, v14
	v_and_b32_e32 v13, 0xffff0000, v14
	v_lshlrev_b32_e32 v14, 16, v15
	v_and_b32_e32 v15, 0xffff0000, v15
	v_mul_f32_e32 v3, v3, v15
	v_mul_f32_e32 v8, v16, v8
	v_mul_f32_e32 v9, v17, v9
	v_mul_f32_e32 v6, v6, v10
	v_mul_f32_e32 v7, v7, v11
	v_mul_f32_e32 v10, v0, v12
	v_mul_f32_e32 v11, v1, v13
	v_mul_f32_e32 v12, v2, v14
	v_cvt_pk_bf16_f32 v0, v8, v9
	v_cvt_pk_bf16_f32 v1, v6, v7
	v_cvt_pk_bf16_f32 v2, v10, v11
	v_cvt_pk_bf16_f32 v3, v12, v3
	global_store_dwordx4 v[4:5], v[0:3], off offset:256
	s_cbranch_vccnz .LBB0_2213
	s_andn2_b64 vcc, exec, s[4:5]
	s_cbranch_vccnz .LBB0_2212
	s_barrier
	s_branch .LBB0_2212
